# conc hi/lo split via one v_fma_mixlo_f16; scalar fast exit for steps in which no reaction block ends
# speedup vs baseline: 1.0115x; 1.0092x over previous
.LBB1_143:
	s_or_b64 exec, exec, s[2:3]
	v_cndmask_b32_e64 v24, v14, 0, s[4:5]
	v_ashrrev_i32_e32 v25, 31, v24
	v_lshlrev_b64 v[24:25], 3, v[24:25]
	s_mov_b64 s[2:3], src_shared_base
	v_lshl_add_u64 v[24:25], s[56:57], 0, v[24:25]
	v_mov_b32_e32 v14, s3
	v_cndmask_b32_e64 v232, v24, 0, s[4:5]
	v_add_lshl_u32 v24, s13, v1, 1
	v_cndmask_b32_e64 v233, v25, v14, s[4:5]
	s_mov_b32 s81, s4
	v_ashrrev_i32_e32 v25, 31, v24
	v_lshl_add_u64 v[24:25], v[24:25], 2, v[232:233]
	flat_load_dwordx2 v[82:83], v[24:25]
	s_mov_b32 s2, 0x4038aa3b
	v_add_f32_e32 v239, s33, v11
	s_waitcnt vmcnt(0)
	v_fma_mixlo_f16 v11, v18, s2, 0
	v_fma_mixlo_f16 v25, v16, s2, 0
	v_fma_mixlo_f16 v27, v17, s2, 0
	v_add_lshl_u32 v22, s13, v22, 1
	v_fma_mixlo_f16 v14, v19, s2, 0
	v_fma_mixlo_f16 v18, v18, s2, -v11 op_sel_hi:[0,0,1]
	v_fma_mixlo_f16 v16, v16, s2, -v25 op_sel_hi:[0,0,1]
	v_fma_mixlo_f16 v17, v17, s2, -v27 op_sel_hi:[0,0,1]
	s_mov_b32 s14, 0x186a0
	v_ashrrev_i32_e32 v23, 31, v22
	v_fma_mixlo_f16 v19, v19, s2, -v14 op_sel_hi:[0,0,1]
	v_cndmask_b32_e64 v11, 0, v11, s[0:1]
	v_cndmask_b32_e64 v14, 0, v14, s[0:1]
	v_cndmask_b32_e64 v25, 0, v25, s[0:1]
	v_cndmask_b32_e64 v27, 0, v27, s[0:1]
	v_cndmask_b32_e64 v18, 0, v18, s[0:1]
	v_cndmask_b32_e64 v16, 0, v16, s[0:1]
	v_cndmask_b32_e64 v17, 0, v17, s[0:1]
	v_pack_b32_f16 v179, v11, v14
	v_pack_b32_f16 v178, v11, v18
	v_pack_b32_f16 v185, v27, v17
	v_pack_b32_f16 v182, v25, v16
	v_lshl_add_u64 v[16:17], v[22:23], 2, v[232:233]
	flat_load_dwordx2 v[236:237], v[16:17]
	v_mov_b32_e32 v17, v2
	v_cndmask_b32_e64 v19, 0, v19, s[0:1]
	v_pack_b32_f16 v180, v19, v14
	v_fma_mixlo_f16 v14, v13, s2, 0
	v_fma_mixlo_f16 v13, v13, s2, -v14 op_sel_hi:[0,0,1]
	v_cndmask_b32_e64 v14, 0, v14, s[0:1]
	v_cndmask_b32_e64 v13, 0, v13, s[0:1]
	v_fma_mixlo_f16 v24, v20, s2, 0
	v_fma_mixlo_f16 v26, v21, s2, 0
	v_or_b32_e32 v240, 64, v1
	v_pack_b32_f16 v188, v13, v14
	v_fma_mixlo_f16 v13, v10, s2, 0
	v_lshl_add_u32 v244, v1, 2, v3
	v_and_b32_e32 v0, 32, v0
	v_mov_b32_e32 v1, 0xa300
	v_fma_mixlo_f16 v20, v20, s2, -v24 op_sel_hi:[0,0,1]
	v_fma_mixlo_f16 v21, v21, s2, -v26 op_sel_hi:[0,0,1]
	v_fma_mixlo_f16 v10, v10, s2, -v13 op_sel_hi:[0,0,1]
	v_lshl_or_b32 v245, v0, 2, v1
	v_lshl_add_u32 v246, v8, 4, v1
	v_add_u32_e32 v3, 64, v7
	v_cndmask_b32_e64 v24, 0, v24, s[0:1]
	v_cndmask_b32_e64 v26, 0, v26, s[0:1]
	v_cndmask_b32_e64 v20, 0, v20, s[0:1]
	v_cndmask_b32_e64 v21, 0, v21, s[0:1]
	v_cndmask_b32_e64 v13, 0, v13, s[0:1]
	v_cndmask_b32_e64 v10, 0, v10, s[0:1]
	v_mov_b32_e32 v0, 0xc0
	v_pack_b32_f16 v183, v25, v26
	v_pack_b32_f16 v181, v24, v20
	v_pack_b32_f16 v184, v21, v26
	v_pack_b32_f16 v193, v13, v10
	v_lshlrev_b32_e32 v251, 3, v9
	v_mov_b32_e32 v7, v2
	v_mov_b32_e32 v9, v2
	v_mov_b32_e32 v10, v2
	v_mov_b32_e32 v13, v2
	v_add_u32_e32 v242, 8, v251
	s_waitcnt lgkmcnt(0)
	v_sub_u32_e32 v234, v231, v230
	s_mov_b64 s[4:5], 0
	v_mov_b32_e32 v249, s6
	s_mov_b32 s71, s6
	v_mov_b32_e32 v231, s13
	s_mov_b32 s15, 0x5040100
	s_mov_b32 s82, 1.0
	s_mov_b32 s83, 1.0
	s_mov_b32 s73, 0x3c000000
	s_mov_b32 s74, 0x42004000
	s_mov_b32 s75, 0x48804800
	s_mov_b32 s76, 0x49804900
	s_mov_b32 s77, 0x4c404c00
	s_mov_b32 s78, 0x4cc04c80
	s_mov_b32 s79, 0x4e404e00
	s_mov_b32 s80, 0x4ec04e80
	v_mov_b32_e32 v197, 0x3c003c00
	s_mov_b32 s16, 0x10000
	s_mov_b32 s17, 0x7a100
	v_lshl_or_b32 v11, v82, 3, 3
	v_cmp_gt_u32_e32 vcc, s14, v82
	v_mov_b32_e32 v196, v83
	s_nop 0
	v_cndmask_b32_e32 v16, 3, v11, vcc
	v_lshl_add_u64 v[16:17], v[16:17], 2, s[54:55]
	global_load_dword v241, v[16:17], off
	v_fma_mixlo_f16 v11, v12, s2, 0
	v_fma_mixlo_f16 v12, v12, s2, -v11 op_sel_hi:[0,0,1]
	v_cndmask_b32_e64 v11, 0, v11, s[0:1]
	v_cndmask_b32_e64 v12, 0, v12, s[0:1]
	v_pack_b32_f16 v187, v11, v14
	v_pack_b32_f16 v186, v11, v12
	v_fma_mixlo_f16 v11, v4, s2, 0
	v_fma_mixlo_f16 v4, v4, s2, -v11 op_sel_hi:[0,0,1]
	v_cndmask_b32_e64 v11, 0, v11, s[0:1]
	v_cndmask_b32_e64 v4, 0, v4, s[0:1]
	v_fma_mixlo_f16 v16, v15, s2, 0
	v_pack_b32_f16 v190, v11, v4
	v_lshrrev_b32_e32 v4, 3, v8
	v_fma_mixlo_f16 v15, v15, s2, -v16 op_sel_hi:[0,0,1]
	v_fma_mixlo_f16 v12, v5, s2, 0
	v_and_b32_e32 v243, 4, v4
	v_cndmask_b32_e64 v16, 0, v16, s[0:1]
	v_cndmask_b32_e64 v15, 0, v15, s[0:1]
	v_fma_mixlo_f16 v5, v5, s2, -v12 op_sel_hi:[0,0,1]
	v_lshl_add_u32 v247, v243, 6, v1
	v_xor_b32_e32 v1, 32, v6
	v_pack_b32_f16 v189, v16, v15
	v_cndmask_b32_e64 v12, 0, v12, s[0:1]
	v_cndmask_b32_e64 v5, 0, v5, s[0:1]
	v_cmp_lt_i32_e32 vcc, v1, v3
	v_mov_b32_e32 v16, v2
	v_mov_b32_e32 v17, v2
	v_pack_b32_f16 v191, v11, v12
	v_pack_b32_f16 v192, v5, v12
	v_lshl_or_b32 v0, v4, 6, v0
	v_cndmask_b32_e32 v1, v6, v1, vcc
	v_mov_b32_e32 v3, v2
	v_mov_b32_e32 v4, v2
	v_mov_b32_e32 v5, v2
	v_mov_b32_e32 v6, v2
	v_mov_b32_e32 v8, v2
	v_mov_b32_e32 v11, v2
	v_mov_b32_e32 v12, v2
	v_mov_b32_e32 v14, v2
	v_mov_b32_e32 v15, v2
	v_mov_b64_e32 v[32:33], v[16:17]
	v_mov_b64_e32 v[48:49], v[16:17]
	v_mov_b64_e32 v[64:65], v[16:17]
	v_mov_b64_e32 v[80:81], v[16:17]
	v_lshlrev_b32_e32 v248, 2, v1
	v_add_u32_e32 v250, 0xa300, v0
	v_mov_b64_e32 v[30:31], v[14:15]
	v_mov_b64_e32 v[28:29], v[12:13]
	v_mov_b64_e32 v[26:27], v[10:11]
	v_mov_b64_e32 v[24:25], v[8:9]
	v_mov_b64_e32 v[22:23], v[6:7]
	v_mov_b64_e32 v[20:21], v[4:5]
	v_mov_b64_e32 v[18:19], v[2:3]
	v_mov_b64_e32 v[46:47], v[14:15]
	v_mov_b64_e32 v[44:45], v[12:13]
	v_mov_b64_e32 v[42:43], v[10:11]
	v_mov_b64_e32 v[40:41], v[8:9]
	v_mov_b64_e32 v[38:39], v[6:7]
	v_mov_b64_e32 v[36:37], v[4:5]
	v_mov_b64_e32 v[34:35], v[2:3]
	v_mov_b64_e32 v[62:63], v[14:15]
	v_mov_b64_e32 v[60:61], v[12:13]
	v_mov_b64_e32 v[58:59], v[10:11]
	v_mov_b64_e32 v[56:57], v[8:9]
	v_mov_b64_e32 v[54:55], v[6:7]
	v_mov_b64_e32 v[52:53], v[4:5]
	v_mov_b64_e32 v[50:51], v[2:3]
	v_mov_b64_e32 v[78:79], v[14:15]
	v_mov_b64_e32 v[76:77], v[12:13]
	v_mov_b64_e32 v[74:75], v[10:11]
	v_mov_b64_e32 v[72:73], v[8:9]
	v_mov_b64_e32 v[70:71], v[6:7]
	v_mov_b64_e32 v[68:69], v[4:5]
	v_mov_b64_e32 v[66:67], v[2:3]
	s_branch .LBB1_145

.LBB1_145:
	s_setprio 0
	s_waitcnt vmcnt(0)
	v_cvt_pk_f16_f32 v194, v241, v241
	v_cmp_gt_u32_e32 vcc, s14, v236
	v_lshl_or_b32 v4, v236, 5, 12
	v_fma_mixlo_f16 v3, v241, 1.0, -v194 op_sel_hi:[0,0,1]
	v_cndmask_b32_e32 v4, 12, v4, vcc
	v_perm_b32 v195, v196, v3, s15
	s_cmp_lg_u32 s81, 0
	s_cbranch_scc0 .Lslow_cs
	v_add_lshl_u32 v6, s13, v240, 3
	ds_read_b64 v[0:1], v6
.Lcs_done:
	global_load_dword v241, v4, s[54:55]
	s_add_i32 s18, s13, 32
	s_add_i32 s19, s13, 16
	s_mov_b64 s[6:7], 0
	v_mfma_f32_32x32x16_f16 v[82:97], v[194:197], v[178:181], 0
	v_mfma_f32_32x32x16_f16 v[98:113], v[194:197], v[182:185], 0
	v_add_u32_e32 v14, s13, v243
	v_sub_u32_e32 v3, v230, v14
	v_add_u32_e32 v4, v3, v234
	v_add_u32_e32 v5, -1, v3
	v_med3_i32 v4, v4, -1, 32
	v_med3_i32 v5, v5, -1, 32
	v_cvt_f32_i32_e32 v4, v4
	v_cvt_f32_i32_e32 v5, v5
	v_cvt_pk_f16_f32 v14, v4, v4
	v_cvt_pk_f16_f32 v15, v5, v5
	v_pk_add_f16 v3, v14, s73 neg_lo:[0,1] neg_hi:[0,1]
	v_pk_add_f16 v4, s73, v15 neg_lo:[0,1] neg_hi:[0,1]
	v_pk_min_f16 v6, v3, v4 clamp
	v_pk_add_f16 v5, v14, s74 neg_lo:[0,1] neg_hi:[0,1]
	v_pk_add_f16 v16, s74, v15 neg_lo:[0,1] neg_hi:[0,1]
	v_pk_min_f16 v7, v5, v16 clamp
	v_pk_add_f16 v3, v14, s75 neg_lo:[0,1] neg_hi:[0,1]
	v_pk_add_f16 v4, s75, v15 neg_lo:[0,1] neg_hi:[0,1]
	v_pk_min_f16 v8, v3, v4 clamp
	v_pk_add_f16 v5, v14, s76 neg_lo:[0,1] neg_hi:[0,1]
	v_pk_add_f16 v16, s76, v15 neg_lo:[0,1] neg_hi:[0,1]
	v_pk_min_f16 v9, v5, v16 clamp
	v_pk_add_f16 v3, v14, s77 neg_lo:[0,1] neg_hi:[0,1]
	v_pk_add_f16 v4, s77, v15 neg_lo:[0,1] neg_hi:[0,1]
	v_pk_min_f16 v10, v3, v4 clamp
	v_pk_add_f16 v5, v14, s78 neg_lo:[0,1] neg_hi:[0,1]
	v_pk_add_f16 v16, s78, v15 neg_lo:[0,1] neg_hi:[0,1]
	v_pk_min_f16 v11, v5, v16 clamp
	v_pk_add_f16 v3, v14, s79 neg_lo:[0,1] neg_hi:[0,1]
	v_pk_add_f16 v4, s79, v15 neg_lo:[0,1] neg_hi:[0,1]
	v_pk_min_f16 v12, v3, v4 clamp
	v_pk_add_f16 v5, v14, s80 neg_lo:[0,1] neg_hi:[0,1]
	v_pk_add_f16 v16, s80, v15 neg_lo:[0,1] neg_hi:[0,1]
	v_pk_min_f16 v13, v5, v16 clamp
	v_exp_f32_e32 v82, v82
	v_exp_f32_e32 v83, v83
	v_exp_f32_e32 v84, v84
	v_exp_f32_e32 v85, v85
	v_exp_f32_e32 v86, v86
	v_exp_f32_e32 v87, v87
	v_exp_f32_e32 v88, v88
	v_exp_f32_e32 v89, v89
	v_exp_f32_e32 v90, v90
	v_exp_f32_e32 v91, v91
	v_exp_f32_e32 v92, v92
	v_exp_f32_e32 v93, v93
	v_exp_f32_e32 v94, v94
	v_exp_f32_e32 v95, v95
	v_exp_f32_e32 v96, v96
	v_exp_f32_e32 v97, v97
	v_pk_add_f32 v[82:83], v[82:83], s[82:83]
	v_pk_add_f32 v[84:85], v[84:85], s[82:83]
	v_pk_add_f32 v[86:87], v[86:87], s[82:83]
	v_pk_add_f32 v[88:89], v[88:89], s[82:83]
	v_pk_add_f32 v[90:91], v[90:91], s[82:83]
	v_pk_add_f32 v[92:93], v[92:93], s[82:83]
	v_pk_add_f32 v[94:95], v[94:95], s[82:83]
	v_pk_add_f32 v[96:97], v[96:97], s[82:83]
	v_rcp_f32_e32 v82, v82
	v_rcp_f32_e32 v83, v83
	v_rcp_f32_e32 v84, v84
	v_rcp_f32_e32 v85, v85
	v_rcp_f32_e32 v86, v86
	v_rcp_f32_e32 v87, v87
	v_rcp_f32_e32 v88, v88
	v_rcp_f32_e32 v89, v89
	v_rcp_f32_e32 v90, v90
	v_rcp_f32_e32 v91, v91
	v_rcp_f32_e32 v92, v92
	v_rcp_f32_e32 v93, v93
	v_rcp_f32_e32 v94, v94
	v_rcp_f32_e32 v95, v95
	v_rcp_f32_e32 v96, v96
	v_rcp_f32_e32 v97, v97
	v_cvt_pk_f16_f32 v198, v82, v83
	v_cvt_pk_f16_f32 v199, v84, v85
	v_cvt_pk_f16_f32 v200, v86, v87
	v_cvt_pk_f16_f32 v201, v88, v89
	v_cvt_pk_f16_f32 v202, v90, v91
	v_cvt_pk_f16_f32 v203, v92, v93
	v_cvt_pk_f16_f32 v204, v94, v95
	v_cvt_pk_f16_f32 v205, v96, v97
	v_mfma_f32_32x32x16_f16 v[82:97], v[194:197], v[186:189], 0
	v_exp_f32_e32 v98, v98
	v_exp_f32_e32 v99, v99
	v_exp_f32_e32 v100, v100
	v_exp_f32_e32 v101, v101
	v_exp_f32_e32 v102, v102
	v_exp_f32_e32 v103, v103
	v_mfma_f32_32x32x16_f16 v[66:81], v[198:201], v[6:9], v[66:81]
	v_exp_f32_e32 v104, v104
	v_exp_f32_e32 v105, v105
	v_exp_f32_e32 v106, v106
	v_exp_f32_e32 v107, v107
	v_exp_f32_e32 v108, v108
	v_exp_f32_e32 v109, v109
	v_mfma_f32_32x32x16_f16 v[66:81], v[202:205], v[10:13], v[66:81]
	v_exp_f32_e32 v110, v110
	v_exp_f32_e32 v111, v111
	v_exp_f32_e32 v112, v112
	v_exp_f32_e32 v113, v113
	v_pk_add_f32 v[98:99], v[98:99], s[82:83]
	v_pk_add_f32 v[100:101], v[100:101], s[82:83]
	v_pk_add_f32 v[102:103], v[102:103], s[82:83]
	v_pk_add_f32 v[104:105], v[104:105], s[82:83]
	v_pk_add_f32 v[106:107], v[106:107], s[82:83]
	v_pk_add_f32 v[108:109], v[108:109], s[82:83]
	v_pk_add_f32 v[110:111], v[110:111], s[82:83]
	v_pk_add_f32 v[112:113], v[112:113], s[82:83]
	v_rcp_f32_e32 v98, v98
	v_rcp_f32_e32 v99, v99
	v_rcp_f32_e32 v100, v100
	v_rcp_f32_e32 v101, v101
	v_rcp_f32_e32 v102, v102
	v_rcp_f32_e32 v103, v103
	v_rcp_f32_e32 v104, v104
	v_rcp_f32_e32 v105, v105
	v_rcp_f32_e32 v106, v106
	v_rcp_f32_e32 v107, v107
	v_rcp_f32_e32 v108, v108
	v_rcp_f32_e32 v109, v109
	v_rcp_f32_e32 v110, v110
	v_rcp_f32_e32 v111, v111
	v_rcp_f32_e32 v112, v112
	v_rcp_f32_e32 v113, v113
	v_cvt_pk_f16_f32 v206, v98, v99
	v_cvt_pk_f16_f32 v207, v100, v101
	v_cvt_pk_f16_f32 v208, v102, v103
	v_cvt_pk_f16_f32 v209, v104, v105
	v_cvt_pk_f16_f32 v210, v106, v107
	v_cvt_pk_f16_f32 v211, v108, v109
	v_cvt_pk_f16_f32 v212, v110, v111
	v_cvt_pk_f16_f32 v213, v112, v113
	v_mfma_f32_32x32x16_f16 v[98:113], v[194:197], v[190:193], 0
	v_exp_f32_e32 v82, v82
	v_exp_f32_e32 v83, v83
	v_exp_f32_e32 v84, v84
	v_exp_f32_e32 v85, v85
	v_exp_f32_e32 v86, v86
	v_exp_f32_e32 v87, v87
	v_mfma_f32_32x32x16_f16 v[50:65], v[206:209], v[6:9], v[50:65]
	v_exp_f32_e32 v88, v88
	v_exp_f32_e32 v89, v89
	v_exp_f32_e32 v90, v90
	v_exp_f32_e32 v91, v91
	v_exp_f32_e32 v92, v92
	v_exp_f32_e32 v93, v93
	v_mfma_f32_32x32x16_f16 v[50:65], v[210:213], v[10:13], v[50:65]
	v_exp_f32_e32 v94, v94
	v_exp_f32_e32 v95, v95
	v_exp_f32_e32 v96, v96
	v_exp_f32_e32 v97, v97
	v_pk_add_f32 v[82:83], v[82:83], s[82:83]
	v_pk_add_f32 v[84:85], v[84:85], s[82:83]
	v_pk_add_f32 v[86:87], v[86:87], s[82:83]
	v_pk_add_f32 v[88:89], v[88:89], s[82:83]
	v_pk_add_f32 v[90:91], v[90:91], s[82:83]
	v_pk_add_f32 v[92:93], v[92:93], s[82:83]
	v_pk_add_f32 v[94:95], v[94:95], s[82:83]
	v_pk_add_f32 v[96:97], v[96:97], s[82:83]
	v_rcp_f32_e32 v82, v82
	v_rcp_f32_e32 v83, v83
	v_rcp_f32_e32 v84, v84
	v_rcp_f32_e32 v85, v85
	v_rcp_f32_e32 v86, v86
	v_rcp_f32_e32 v87, v87
	v_rcp_f32_e32 v88, v88
	v_rcp_f32_e32 v89, v89
	v_rcp_f32_e32 v90, v90
	v_rcp_f32_e32 v91, v91
	v_rcp_f32_e32 v92, v92
	v_rcp_f32_e32 v93, v93
	v_rcp_f32_e32 v94, v94
	v_rcp_f32_e32 v95, v95
	v_rcp_f32_e32 v96, v96
	v_rcp_f32_e32 v97, v97
	v_cvt_pk_f16_f32 v214, v82, v83
	v_cvt_pk_f16_f32 v215, v84, v85
	v_cvt_pk_f16_f32 v216, v86, v87
	v_cvt_pk_f16_f32 v217, v88, v89
	v_cvt_pk_f16_f32 v218, v90, v91
	v_cvt_pk_f16_f32 v219, v92, v93
	v_cvt_pk_f16_f32 v220, v94, v95
	v_cvt_pk_f16_f32 v221, v96, v97
	v_exp_f32_e32 v98, v98
	v_exp_f32_e32 v99, v99
	v_exp_f32_e32 v100, v100
	v_exp_f32_e32 v101, v101
	v_exp_f32_e32 v102, v102
	v_exp_f32_e32 v103, v103
	v_mfma_f32_32x32x16_f16 v[34:49], v[214:217], v[6:9], v[34:49]
	v_exp_f32_e32 v104, v104
	v_exp_f32_e32 v105, v105
	v_exp_f32_e32 v106, v106
	v_exp_f32_e32 v107, v107
	v_exp_f32_e32 v108, v108
	v_exp_f32_e32 v109, v109
	v_mfma_f32_32x32x16_f16 v[34:49], v[218:221], v[10:13], v[34:49]
	v_exp_f32_e32 v110, v110
	v_exp_f32_e32 v111, v111
	v_exp_f32_e32 v112, v112
	v_exp_f32_e32 v113, v113
	v_pk_add_f32 v[98:99], v[98:99], s[82:83]
	v_pk_add_f32 v[100:101], v[100:101], s[82:83]
	v_pk_add_f32 v[102:103], v[102:103], s[82:83]
	v_pk_add_f32 v[104:105], v[104:105], s[82:83]
	v_pk_add_f32 v[106:107], v[106:107], s[82:83]
	v_pk_add_f32 v[108:109], v[108:109], s[82:83]
	v_pk_add_f32 v[110:111], v[110:111], s[82:83]
	v_pk_add_f32 v[112:113], v[112:113], s[82:83]
	v_rcp_f32_e32 v98, v98
	v_rcp_f32_e32 v99, v99
	v_rcp_f32_e32 v100, v100
	v_rcp_f32_e32 v101, v101
	v_rcp_f32_e32 v102, v102
	v_rcp_f32_e32 v103, v103
	v_rcp_f32_e32 v104, v104
	v_rcp_f32_e32 v105, v105
	v_rcp_f32_e32 v106, v106
	v_rcp_f32_e32 v107, v107
	v_rcp_f32_e32 v108, v108
	v_rcp_f32_e32 v109, v109
	v_rcp_f32_e32 v110, v110
	v_rcp_f32_e32 v111, v111
	v_rcp_f32_e32 v112, v112
	v_rcp_f32_e32 v113, v113
	v_cvt_pk_f16_f32 v222, v98, v99
	v_cvt_pk_f16_f32 v223, v100, v101
	v_cvt_pk_f16_f32 v224, v102, v103
	v_cvt_pk_f16_f32 v225, v104, v105
	v_cvt_pk_f16_f32 v226, v106, v107
	v_cvt_pk_f16_f32 v227, v108, v109
	v_cvt_pk_f16_f32 v228, v110, v111
	v_cvt_pk_f16_f32 v229, v112, v113
	v_mfma_f32_32x32x16_f16 v[18:33], v[222:225], v[6:9], v[18:33]
	v_add_u32_e32 v194, s13, v243
	v_mfma_f32_32x32x16_f16 v[18:33], v[226:229], v[10:13], v[18:33]
	s_cmp_ge_i32 s18, s71
	s_cbranch_scc1 .Lpeel_join
	v_mov_b32_e32 v196, v237
	s_waitcnt vmcnt(0) lgkmcnt(0)
	v_mov_b64_e32 v[236:237], v[0:1]
	s_mov_b32 s13, s18
	s_branch .LBB1_145

.LBB1_146:
	s_or_b64 exec, exec, s[10:11]
	v_mov_b64_e32 v[234:235], v[16:17]
	s_mov_b64 s[10:11], exec
	v_mov_b32_e32 v251, v82
	v_mov_b32_e32 v231, v249
	v_mov_b32_e32 v249, s20
	s_mov_b32 s71, s20
